# baseline (speedup 1.0000x reference)
_Z8k4_fusedPKfPKDF16_S2_S0_S0_S2_S0_S0_Pf:
	v_readfirstlane_b32 s54, v0
	s_nop 0
	s_bfe_u32 s54, s54, 0x10008
	s_cmp_eq_u32 s54, 0
	s_cbranch_scc0 .Lpa_prio_skip
	s_setprio 1
.Lpa_prio_skip:
	s_load_dwordx4 s[4:7], s[0:1], 0x18
	s_load_dwordx2 s[20:21], s[0:1], 0x28
	s_lshr_b32 s8, s2, 7
	v_lshrrev_b32_e32 v101, 8, v0
	v_bfe_u32 v99, v0, 6, 2
	s_mul_i32 s9, s8, 0x2300
	v_lshlrev_b32_e32 v105, 2, v101
	s_mul_hi_u32 s3, s8, 0x2300
	s_waitcnt lgkmcnt(0)
	s_add_u32 s4, s4, s9
	v_or_b32_e32 v1, v105, v99
	v_bfe_u32 v89, v0, 2, 4
	s_addc_u32 s5, s5, s3
	v_lshlrev_b32_e32 v26, 10, v1
	v_mov_b32_e32 v27, 0
	v_and_b32_e32 v90, 3, v0
	v_lshl_add_u64 v[2:3], s[4:5], 0, v[26:27]
	v_lshlrev_b32_e32 v4, 6, v89
	v_mov_b32_e32 v5, v27
	v_lshl_add_u64 v[2:3], v[2:3], 0, v[4:5]
	v_lshlrev_b32_e32 v4, 4, v90
	v_lshl_add_u64 v[10:11], v[2:3], 0, v[4:5]
	v_and_b32_e32 v2, 0x100, v0
	v_mov_b32_e32 v3, v27
	v_lshl_add_u64 v[2:3], s[4:5], 0, v[2:3]
	v_lshlrev_b32_e32 v6, 6, v99
	v_mov_b32_e32 v7, v27
	v_lshl_add_u64 v[2:3], v[2:3], 0, v[6:7]
	v_lshlrev_b32_e32 v104, 4, v99
	v_lshl_add_u64 v[2:3], v[2:3], 0, v[4:5]
	s_movk_i32 s3, 0x2000
	v_add_co_u32_e32 v12, vcc, s3, v2
	v_or_b32_e32 v1, v104, v89
	s_nop 0
	v_addc_co_u32_e32 v13, vcc, 0, v3, vcc
	global_load_dwordx4 v[2:5], v[10:11], off
	global_load_dwordx4 v[6:9], v[12:13], off offset:256
	v_lshlrev_b32_e32 v10, 2, v1
	v_mov_b32_e32 v11, v27
	v_lshl_add_u64 v[10:11], s[4:5], 0, v[10:11]
	v_add_co_u32_e32 v10, vcc, s3, v10
	v_lshlrev_b32_e32 v72, 4, v0
	s_nop 0
	v_addc_co_u32_e32 v11, vcc, 0, v11, vcc
	v_mov_b32_e32 v73, v27
	global_load_dword v95, v[10:11], off
	v_lshl_add_u64 v[10:11], s[20:21], 0, v[72:73]
	v_add_co_u32_e32 v10, vcc, 0x8000, v10
	v_lshlrev_b32_e32 v1, 2, v99
	s_nop 0
	v_addc_co_u32_e32 v11, vcc, 0, v11, vcc
	global_load_dword v91, v1, s[6:7]
	s_mov_b32 s9, 0
	global_load_dwordx4 v[10:13], v[10:11], off offset:2304
	v_cmp_gt_u32_e64 s[4:5], 64, v0
	v_lshlrev_b32_e32 v96, 2, v0
	v_mov_b32_e32 v97, v27
	s_and_saveexec_b64 s[6:7], s[4:5]
	s_cbranch_execz .LBB4_2
	s_load_dwordx4 s[12:15], s[0:1], 0x30
	s_waitcnt lgkmcnt(0)
	global_load_dword v97, v96, s[12:13]
	global_load_dword v27, v96, s[14:15]

.Lp1_smap_done:
	v_and_b32_e32 v94, 1, v99
	v_lshl_or_b32 v96, v94, 6, v103
	s_movk_i32 s100, 0x90
	v_mad_u32_u24 v88, v88, s100, v96
	v_mad_u32_u24 v90, v90, s100, v96
	v_mad_u32_u24 v92, v92, s100, v96
	v_lshl_add_u32 v86, v94, 12, v75
	s_movk_i32 s100, 0x1800
	v_mad_u32_u24 v96, v85, s100, v84
	ds_read_b128 v[40:43], v96
	ds_read_b128 v[44:47], v96 offset:1024
	ds_read_b128 v[48:51], v96 offset:2048
	ds_read_b128 v[52:55], v96 offset:3072
	ds_read_b128 v[56:59], v96 offset:4096
	ds_read_b128 v[60:63], v96 offset:5120
	s_lshr_b32 s101, s18, 8
	s_waitcnt lgkmcnt(0)
	s_mov_b32 s100, 0x3f596d27
	s_setprio 0
	s_branch .LBB4_37
